# routing stage 1: LDS bank conflict removed, the odd thread of a list reads its half rotated by 32 dwords
# baseline (speedup 1.0000x reference)
; DI void routing_block(LAS unsigned char* lds, const bf16* q, const bf16* skb, int* experts, float* pgates, int tb) {
;     ...
;         const int t0 = tb * 32, hc = 8 * hp + wave;
;         f32x16 acc[4];
; #pragma unroll
;         for (int kb = 0; kb < 4; ++kb)
; #pragma unroll
;             for (int i = 0; i < 16; ++i) acc[kb][i] = 0.f;
; #pragma unroll
;         for (int ks = 0; ks < 8; ++ks) {
;             const bf16x8 a = *(const bf16x8*)(q + (size_t)(t0 + r) * QW + hc * 128 + 16 * ks + 8 * h);
; #pragma unroll
;             for (int kb = 0; kb < 4; ++kb) {
;                 const bf16x8 b = *(const bf16x8*)(skb + ((size_t)hc * 128 + 32 * kb + r) * 128 + 16 * ks + 8 * h);
;                 acc[kb] = __builtin_amdgcn_mfma_f32_32x32x16_bf16(a, b, acc[kb], 0, 0, 0);
;             }
;         }
.LBB0_894:
	s_lshl_b32 s76, s78, 3
	s_add_i32 s76, s76, s79
	s_lshl_b32 vcc_lo, s76, 7
	s_ashr_i32 vcc_hi, vcc_lo, 31
	v_lshl_add_u64 v[110:111], vcc, 1, v[80:81]
	s_ashr_i32 s77, s76, 31
	global_load_dwordx4 v[146:149], v[110:111], off
	global_load_dwordx4 v[150:153], v[110:111], off offset:32
	global_load_dwordx4 v[154:157], v[110:111], off offset:64
	global_load_dwordx4 v[158:161], v[110:111], off offset:96
	global_load_dwordx4 v[162:165], v[110:111], off offset:128
	global_load_dwordx4 v[166:169], v[110:111], off offset:160
	global_load_dwordx4 v[170:173], v[110:111], off offset:192
	global_load_dwordx4 v[174:177], v[110:111], off offset:224
	s_lshl_b64 s[76:77], s[76:77], 15
	v_mov_b32_e32 v105, s77
	v_or_b32_e32 v104, s76, v102
	v_lshl_add_u64 v[112:113], v[82:83], 0, v[104:105]
	v_or_b32_e32 v108, 0x2000, v104
	v_mov_b32_e32 v109, s77
	v_or_b32_e32 v106, 0x4000, v104
	v_mov_b32_e32 v107, s77
	v_or_b32_e32 v104, 0x6000, v104
	v_lshl_add_u64 v[242:243], v[82:83], 0, v[108:109]
	v_lshl_add_u64 v[244:245], v[82:83], 0, v[106:107]
	v_lshl_add_u64 v[246:247], v[82:83], 0, v[104:105]
	global_load_dwordx4 v[178:181], v[112:113], off
	global_load_dwordx4 v[182:185], v[242:243], off
	global_load_dwordx4 v[186:189], v[244:245], off
	global_load_dwordx4 v[190:193], v[246:247], off
	global_load_dwordx4 v[194:197], v[112:113], off offset:32
	global_load_dwordx4 v[198:201], v[242:243], off offset:32
	global_load_dwordx4 v[202:205], v[244:245], off offset:32
	global_load_dwordx4 v[206:209], v[246:247], off offset:32
	global_load_dwordx4 v[210:213], v[112:113], off offset:64
	global_load_dwordx4 v[214:217], v[242:243], off offset:64
	global_load_dwordx4 v[218:221], v[244:245], off offset:64
	global_load_dwordx4 v[222:225], v[246:247], off offset:64
	global_load_dwordx4 v[226:229], v[112:113], off offset:96
	global_load_dwordx4 v[230:233], v[242:243], off offset:96
	global_load_dwordx4 v[234:237], v[244:245], off offset:96
	global_load_dwordx4 v[238:241], v[246:247], off offset:96
	s_xor_b64 s[74:75], s[74:75], -1
	s_mov_b32 s76, 0
	s_waitcnt vmcnt(12)
	v_mfma_f32_32x32x16_bf16 v[50:65], v[146:149], v[178:181], 0
	v_mfma_f32_32x32x16_bf16 v[34:49], v[146:149], v[182:185], 0
	v_mfma_f32_32x32x16_bf16 v[18:33], v[146:149], v[186:189], 0
	v_mfma_f32_32x32x16_bf16 v[2:17], v[146:149], v[190:193], 0
	global_load_dwordx4 v[178:181], v[112:113], off offset:128
	global_load_dwordx4 v[182:185], v[242:243], off offset:128
	global_load_dwordx4 v[186:189], v[244:245], off offset:128
	global_load_dwordx4 v[190:193], v[246:247], off offset:128
	s_waitcnt vmcnt(12)
	v_mfma_f32_32x32x16_bf16 v[50:65], v[150:153], v[194:197], v[50:65]
	v_mfma_f32_32x32x16_bf16 v[34:49], v[150:153], v[198:201], v[34:49]
	v_mfma_f32_32x32x16_bf16 v[18:33], v[150:153], v[202:205], v[18:33]
	v_mfma_f32_32x32x16_bf16 v[2:17], v[150:153], v[206:209], v[2:17]
	global_load_dwordx4 v[194:197], v[112:113], off offset:160
	global_load_dwordx4 v[198:201], v[242:243], off offset:160
	global_load_dwordx4 v[202:205], v[244:245], off offset:160
	global_load_dwordx4 v[206:209], v[246:247], off offset:160
	s_waitcnt vmcnt(12)
	v_mfma_f32_32x32x16_bf16 v[50:65], v[154:157], v[210:213], v[50:65]
	v_mfma_f32_32x32x16_bf16 v[34:49], v[154:157], v[214:217], v[34:49]
	v_mfma_f32_32x32x16_bf16 v[18:33], v[154:157], v[218:221], v[18:33]
	v_mfma_f32_32x32x16_bf16 v[2:17], v[154:157], v[222:225], v[2:17]
	global_load_dwordx4 v[210:213], v[112:113], off offset:192
	global_load_dwordx4 v[214:217], v[242:243], off offset:192
	global_load_dwordx4 v[218:221], v[244:245], off offset:192
	global_load_dwordx4 v[222:225], v[246:247], off offset:192
	s_waitcnt vmcnt(12)
	v_mfma_f32_32x32x16_bf16 v[50:65], v[158:161], v[226:229], v[50:65]
	v_mfma_f32_32x32x16_bf16 v[34:49], v[158:161], v[230:233], v[34:49]
	v_mfma_f32_32x32x16_bf16 v[18:33], v[158:161], v[234:237], v[18:33]
	v_mfma_f32_32x32x16_bf16 v[2:17], v[158:161], v[238:241], v[2:17]
	global_load_dwordx4 v[226:229], v[112:113], off offset:224
	global_load_dwordx4 v[230:233], v[242:243], off offset:224
	global_load_dwordx4 v[234:237], v[244:245], off offset:224
	global_load_dwordx4 v[238:241], v[246:247], off offset:224
	s_waitcnt vmcnt(12)
	v_mfma_f32_32x32x16_bf16 v[50:65], v[162:165], v[178:181], v[50:65]
	v_mfma_f32_32x32x16_bf16 v[34:49], v[162:165], v[182:185], v[34:49]
	v_mfma_f32_32x32x16_bf16 v[18:33], v[162:165], v[186:189], v[18:33]
	v_mfma_f32_32x32x16_bf16 v[2:17], v[162:165], v[190:193], v[2:17]
	s_waitcnt vmcnt(8)
	v_mfma_f32_32x32x16_bf16 v[50:65], v[166:169], v[194:197], v[50:65]
	v_mfma_f32_32x32x16_bf16 v[34:49], v[166:169], v[198:201], v[34:49]
	v_mfma_f32_32x32x16_bf16 v[18:33], v[166:169], v[202:205], v[18:33]
	v_mfma_f32_32x32x16_bf16 v[2:17], v[166:169], v[206:209], v[2:17]
	s_waitcnt vmcnt(4)
	v_mfma_f32_32x32x16_bf16 v[50:65], v[170:173], v[210:213], v[50:65]
	v_mfma_f32_32x32x16_bf16 v[34:49], v[170:173], v[214:217], v[34:49]
	v_mfma_f32_32x32x16_bf16 v[18:33], v[170:173], v[218:221], v[18:33]
	v_mfma_f32_32x32x16_bf16 v[2:17], v[170:173], v[222:225], v[2:17]
	s_waitcnt vmcnt(0)
; DI int crow(int reg, int h) { return (reg & 3) + 8 * (reg >> 2) + 4 * h; }
; DI void routing_block(LAS unsigned char* lds, const bf16* q, const bf16* skb, int* experts, float* pgates, int tb) {
;     ...
;             for (int kb = 0; kb < 4; ++kb) {
;                 const bf16x8 b = *(const bf16x8*)(skb + ((size_t)hc * 128 + 32 * kb + r) * 128 + 16 * ks + 8 * h);
;                 acc[kb] = __builtin_amdgcn_mfma_f32_32x32x16_bf16(a, b, acc[kb], 0, 0, 0);
;             }
;         }
; #pragma unroll
;         for (int kb = 0; kb < 4; ++kb)
; #pragma unroll
;             for (int i = 0; i < 16; ++i) {
;                 const int key = 32 * kb + r;
;                 sc[(crow(i, h) * 8 + wave) * RT_PITCH + key] = (f2key(acc[kb][i]) & ~127) | key;
;             }
	v_mfma_f32_32x32x16_bf16 v[50:65], v[174:177], v[226:229], v[50:65]
	v_mfma_f32_32x32x16_bf16 v[34:49], v[174:177], v[230:233], v[34:49]
	v_mfma_f32_32x32x16_bf16 v[18:33], v[174:177], v[234:237], v[18:33]
	v_mfma_f32_32x32x16_bf16 v[2:17], v[174:177], v[238:241], v[2:17]
	s_nop 11
	v_ashrrev_i32_e32 v105, 31, v51
	v_and_b32_e32 v105, 0x7fffff80, v105
	v_and_b32_e32 v51, 0xffffff80, v51
	v_bitop3_b32 v51, v105, v103, v51 bitop3:0xde
	v_ashrrev_i32_e32 v105, 31, v52
	v_and_b32_e32 v105, 0x7fffff80, v105
	v_and_b32_e32 v52, 0xffffff80, v52
	v_bitop3_b32 v52, v105, v103, v52 bitop3:0xde
	v_ashrrev_i32_e32 v105, 31, v53
	v_and_b32_e32 v105, 0x7fffff80, v105
	v_and_b32_e32 v53, 0xffffff80, v53
	v_bitop3_b32 v53, v105, v103, v53 bitop3:0xde
	v_ashrrev_i32_e32 v105, 31, v54
	v_and_b32_e32 v105, 0x7fffff80, v105
	v_and_b32_e32 v54, 0xffffff80, v54
	v_bitop3_b32 v54, v105, v103, v54 bitop3:0xde
	v_ashrrev_i32_e32 v105, 31, v55
	v_and_b32_e32 v105, 0x7fffff80, v105
	v_and_b32_e32 v55, 0xffffff80, v55
	v_bitop3_b32 v55, v105, v103, v55 bitop3:0xde
	v_ashrrev_i32_e32 v105, 31, v56
	v_and_b32_e32 v105, 0x7fffff80, v105
	v_and_b32_e32 v56, 0xffffff80, v56
	v_bitop3_b32 v56, v105, v103, v56 bitop3:0xde
	v_ashrrev_i32_e32 v105, 31, v57
	v_and_b32_e32 v105, 0x7fffff80, v105
	v_and_b32_e32 v57, 0xffffff80, v57
	v_bitop3_b32 v57, v105, v103, v57 bitop3:0xde
	v_ashrrev_i32_e32 v105, 31, v58
	v_and_b32_e32 v105, 0x7fffff80, v105
	v_and_b32_e32 v58, 0xffffff80, v58
	v_bitop3_b32 v58, v105, v103, v58 bitop3:0xde
	v_ashrrev_i32_e32 v105, 31, v59
	v_and_b32_e32 v105, 0x7fffff80, v105
	v_and_b32_e32 v59, 0xffffff80, v59
	v_bitop3_b32 v59, v105, v103, v59 bitop3:0xde
	v_ashrrev_i32_e32 v105, 31, v60
	v_and_b32_e32 v105, 0x7fffff80, v105
	v_and_b32_e32 v60, 0xffffff80, v60
	v_bitop3_b32 v60, v105, v103, v60 bitop3:0xde
	v_ashrrev_i32_e32 v105, 31, v61
	v_and_b32_e32 v105, 0x7fffff80, v105
	v_and_b32_e32 v61, 0xffffff80, v61
	v_bitop3_b32 v61, v105, v103, v61 bitop3:0xde
	v_ashrrev_i32_e32 v105, 31, v62
	v_and_b32_e32 v105, 0x7fffff80, v105
	v_and_b32_e32 v62, 0xffffff80, v62
	v_bitop3_b32 v62, v105, v103, v62 bitop3:0xde
	v_ashrrev_i32_e32 v105, 31, v63
	v_and_b32_e32 v105, 0x7fffff80, v105
	v_and_b32_e32 v63, 0xffffff80, v63
	v_bitop3_b32 v63, v105, v103, v63 bitop3:0xde
	v_ashrrev_i32_e32 v105, 31, v64
	v_and_b32_e32 v105, 0x7fffff80, v105
	v_and_b32_e32 v64, 0xffffff80, v64
	v_bitop3_b32 v64, v105, v103, v64 bitop3:0xde
	v_ashrrev_i32_e32 v105, 31, v65
	v_and_b32_e32 v105, 0x7fffff80, v105
	v_and_b32_e32 v65, 0xffffff80, v65
	v_ashrrev_i32_e32 v104, 31, v50
	v_bitop3_b32 v65, v105, v103, v65 bitop3:0xde
	v_ashrrev_i32_e32 v105, 31, v34
	v_and_b32_e32 v104, 0x7fffff80, v104
	v_and_b32_e32 v50, 0xffffff80, v50
	v_and_b32_e32 v105, 0x7fffff80, v105
	v_and_b32_e32 v34, 0xffffff80, v34
	v_bitop3_b32 v50, v104, v103, v50 bitop3:0xde
	v_add_u32_e32 v104, v123, v124
	v_bitop3_b32 v34, v105, v125, v34 bitop3:0xde
	ds_write2_b32 v104, v50, v34 offset1:32
	v_ashrrev_i32_e32 v34, 31, v35
	v_and_b32_e32 v34, 0x7fffff80, v34
	v_and_b32_e32 v35, 0xffffff80, v35
	v_bitop3_b32 v34, v34, v125, v35 bitop3:0xde
	v_add_u32_e32 v35, 0x1000, v104
	ds_write2_b32 v35, v51, v34 offset0:8 offset1:40
	v_ashrrev_i32_e32 v34, 31, v36
	v_and_b32_e32 v34, 0x7fffff80, v34
	v_and_b32_e32 v36, 0xffffff80, v36
	v_bitop3_b32 v34, v34, v125, v36 bitop3:0xde
	v_add_u32_e32 v36, 0x2000, v104
	ds_write2_b32 v36, v52, v34 offset0:16 offset1:48
	v_ashrrev_i32_e32 v34, 31, v37
	v_and_b32_e32 v34, 0x7fffff80, v34
	v_and_b32_e32 v37, 0xffffff80, v37
	v_bitop3_b32 v34, v34, v125, v37 bitop3:0xde
	v_add_u32_e32 v37, 0x3000, v104
	ds_write2_b32 v37, v53, v34 offset0:24 offset1:56
	v_ashrrev_i32_e32 v34, 31, v38
	v_and_b32_e32 v34, 0x7fffff80, v34
	v_and_b32_e32 v38, 0xffffff80, v38
	v_bitop3_b32 v34, v34, v125, v38 bitop3:0xde
	v_add_u32_e32 v38, 0x8000, v104
	ds_write2_b32 v38, v54, v34 offset0:64 offset1:96
	v_ashrrev_i32_e32 v34, 31, v39
	v_and_b32_e32 v34, 0x7fffff80, v34
	v_and_b32_e32 v39, 0xffffff80, v39
	v_bitop3_b32 v34, v34, v125, v39 bitop3:0xde
	v_add_u32_e32 v39, 0x9000, v104
	ds_write2_b32 v39, v55, v34 offset0:72 offset1:104
	v_ashrrev_i32_e32 v34, 31, v40
	v_and_b32_e32 v34, 0x7fffff80, v34
	v_and_b32_e32 v40, 0xffffff80, v40
	v_bitop3_b32 v34, v34, v125, v40 bitop3:0xde
	v_add_u32_e32 v40, 0xa000, v104
	ds_write2_b32 v40, v56, v34 offset0:80 offset1:112
	v_ashrrev_i32_e32 v34, 31, v41
	v_and_b32_e32 v34, 0x7fffff80, v34
	v_and_b32_e32 v41, 0xffffff80, v41
	v_bitop3_b32 v34, v34, v125, v41 bitop3:0xde
	v_add_u32_e32 v41, 0xb000, v104
	ds_write2_b32 v41, v57, v34 offset0:88 offset1:120
	v_ashrrev_i32_e32 v34, 31, v42
	v_and_b32_e32 v34, 0x7fffff80, v34
	v_and_b32_e32 v42, 0xffffff80, v42
	v_bitop3_b32 v34, v34, v125, v42 bitop3:0xde
	ds_write2_b32 v128, v58, v34 offset1:32
	v_ashrrev_i32_e32 v34, 31, v43
	v_and_b32_e32 v34, 0x7fffff80, v34
	v_and_b32_e32 v42, 0xffffff80, v43
	v_bitop3_b32 v34, v34, v125, v42 bitop3:0xde
	ds_write2_b32 v129, v59, v34 offset1:32
	v_ashrrev_i32_e32 v34, 31, v44
	v_and_b32_e32 v34, 0x7fffff80, v34
	v_and_b32_e32 v42, 0xffffff80, v44
	v_bitop3_b32 v34, v34, v125, v42 bitop3:0xde
	ds_write2_b32 v130, v60, v34 offset1:32
	v_ashrrev_i32_e32 v34, 31, v45
	v_and_b32_e32 v34, 0x7fffff80, v34
	v_and_b32_e32 v42, 0xffffff80, v45
	v_bitop3_b32 v34, v34, v125, v42 bitop3:0xde
	ds_write2_b32 v131, v61, v34 offset1:32
	v_ashrrev_i32_e32 v34, 31, v46
	v_and_b32_e32 v34, 0x7fffff80, v34
	v_and_b32_e32 v42, 0xffffff80, v46
	v_bitop3_b32 v34, v34, v125, v42 bitop3:0xde
	ds_write2_b32 v132, v62, v34 offset1:32
	v_ashrrev_i32_e32 v34, 31, v47
	v_and_b32_e32 v34, 0x7fffff80, v34
; DI int crow(int reg, int h) { return (reg & 3) + 8 * (reg >> 2) + 4 * h; }
; DI void routing_block(LAS unsigned char* lds, const bf16* q, const bf16* skb, int* experts, float* pgates, int tb) {
;     ...
; #pragma unroll
;         for (int kb = 0; kb < 4; ++kb)
; #pragma unroll
;             for (int i = 0; i < 16; ++i) {
;                 const int key = 32 * kb + r;
;                 sc[(crow(i, h) * 8 + wave) * RT_PITCH + key] = (f2key(acc[kb][i]) & ~127) | key;
;             }
;         __syncthreads();
	v_and_b32_e32 v42, 0xffffff80, v47
	v_bitop3_b32 v34, v34, v125, v42 bitop3:0xde
	ds_write2_b32 v133, v63, v34 offset1:32
	v_ashrrev_i32_e32 v34, 31, v48
	v_and_b32_e32 v34, 0x7fffff80, v34
	v_and_b32_e32 v42, 0xffffff80, v48
	v_bitop3_b32 v34, v34, v125, v42 bitop3:0xde
	ds_write2_b32 v134, v64, v34 offset1:32
	v_ashrrev_i32_e32 v34, 31, v49
	v_and_b32_e32 v34, 0x7fffff80, v34
	v_and_b32_e32 v42, 0xffffff80, v49
	v_bitop3_b32 v34, v34, v125, v42 bitop3:0xde
	ds_write2_b32 v135, v65, v34 offset1:32
	v_ashrrev_i32_e32 v34, 31, v18
	v_and_b32_e32 v34, 0x7fffff80, v34
	v_and_b32_e32 v18, 0xffffff80, v18
	v_bitop3_b32 v18, v34, v126, v18 bitop3:0xde
	v_ashrrev_i32_e32 v34, 31, v19
	v_and_b32_e32 v34, 0x7fffff80, v34
	v_and_b32_e32 v19, 0xffffff80, v19
	v_bitop3_b32 v19, v34, v126, v19 bitop3:0xde
	v_ashrrev_i32_e32 v34, 31, v20
	v_and_b32_e32 v34, 0x7fffff80, v34
	v_and_b32_e32 v20, 0xffffff80, v20
	v_bitop3_b32 v20, v34, v126, v20 bitop3:0xde
	v_ashrrev_i32_e32 v34, 31, v21
	v_and_b32_e32 v34, 0x7fffff80, v34
	v_and_b32_e32 v21, 0xffffff80, v21
	v_bitop3_b32 v21, v34, v126, v21 bitop3:0xde
	v_ashrrev_i32_e32 v34, 31, v22
	v_and_b32_e32 v34, 0x7fffff80, v34
	v_and_b32_e32 v22, 0xffffff80, v22
	v_bitop3_b32 v22, v34, v126, v22 bitop3:0xde
	v_ashrrev_i32_e32 v34, 31, v23
	v_and_b32_e32 v34, 0x7fffff80, v34
	v_and_b32_e32 v23, 0xffffff80, v23
	v_bitop3_b32 v23, v34, v126, v23 bitop3:0xde
	v_ashrrev_i32_e32 v34, 31, v24
	v_and_b32_e32 v34, 0x7fffff80, v34
	v_and_b32_e32 v24, 0xffffff80, v24
	v_bitop3_b32 v24, v34, v126, v24 bitop3:0xde
	v_ashrrev_i32_e32 v34, 31, v25
	v_and_b32_e32 v34, 0x7fffff80, v34
	v_and_b32_e32 v25, 0xffffff80, v25
	v_bitop3_b32 v25, v34, v126, v25 bitop3:0xde
	v_ashrrev_i32_e32 v34, 31, v26
	v_and_b32_e32 v34, 0x7fffff80, v34
	v_and_b32_e32 v26, 0xffffff80, v26
	v_bitop3_b32 v26, v34, v126, v26 bitop3:0xde
	v_ashrrev_i32_e32 v34, 31, v27
	v_and_b32_e32 v34, 0x7fffff80, v34
	v_and_b32_e32 v27, 0xffffff80, v27
	v_bitop3_b32 v27, v34, v126, v27 bitop3:0xde
	v_ashrrev_i32_e32 v34, 31, v28
	v_and_b32_e32 v34, 0x7fffff80, v34
	v_and_b32_e32 v28, 0xffffff80, v28
	v_bitop3_b32 v28, v34, v126, v28 bitop3:0xde
	v_ashrrev_i32_e32 v34, 31, v29
	v_and_b32_e32 v34, 0x7fffff80, v34
	v_and_b32_e32 v29, 0xffffff80, v29
	v_bitop3_b32 v29, v34, v126, v29 bitop3:0xde
	v_ashrrev_i32_e32 v34, 31, v30
	v_and_b32_e32 v34, 0x7fffff80, v34
	v_and_b32_e32 v30, 0xffffff80, v30
	v_bitop3_b32 v30, v34, v126, v30 bitop3:0xde
	v_ashrrev_i32_e32 v34, 31, v31
	v_and_b32_e32 v34, 0x7fffff80, v34
	v_and_b32_e32 v31, 0xffffff80, v31
	v_bitop3_b32 v31, v34, v126, v31 bitop3:0xde
	v_ashrrev_i32_e32 v34, 31, v32
	v_and_b32_e32 v34, 0x7fffff80, v34
	v_and_b32_e32 v32, 0xffffff80, v32
	v_bitop3_b32 v32, v34, v126, v32 bitop3:0xde
	v_ashrrev_i32_e32 v34, 31, v33
	v_and_b32_e32 v34, 0x7fffff80, v34
	v_and_b32_e32 v33, 0xffffff80, v33
	v_bitop3_b32 v33, v34, v126, v33 bitop3:0xde
	v_ashrrev_i32_e32 v34, 31, v2
	v_and_b32_e32 v34, 0x7fffff80, v34
	v_and_b32_e32 v2, 0xffffff80, v2
	v_bitop3_b32 v2, v34, v127, v2 bitop3:0xde
	ds_write2_b32 v104, v18, v2 offset0:64 offset1:96
	v_ashrrev_i32_e32 v2, 31, v3
	v_and_b32_e32 v2, 0x7fffff80, v2
	v_and_b32_e32 v3, 0xffffff80, v3
	v_bitop3_b32 v2, v2, v127, v3 bitop3:0xde
	ds_write2_b32 v35, v19, v2 offset0:72 offset1:104
	v_ashrrev_i32_e32 v2, 31, v4
	v_and_b32_e32 v2, 0x7fffff80, v2
	v_and_b32_e32 v3, 0xffffff80, v4
	v_bitop3_b32 v2, v2, v127, v3 bitop3:0xde
	ds_write2_b32 v36, v20, v2 offset0:80 offset1:112
	v_ashrrev_i32_e32 v2, 31, v5
	v_and_b32_e32 v2, 0x7fffff80, v2
	v_and_b32_e32 v3, 0xffffff80, v5
	v_bitop3_b32 v2, v2, v127, v3 bitop3:0xde
	ds_write2_b32 v37, v21, v2 offset0:88 offset1:120
	v_ashrrev_i32_e32 v2, 31, v6
	v_and_b32_e32 v2, 0x7fffff80, v2
	v_and_b32_e32 v3, 0xffffff80, v6
	v_bitop3_b32 v2, v2, v127, v3 bitop3:0xde
	ds_write2_b32 v38, v22, v2 offset0:128 offset1:160
	v_ashrrev_i32_e32 v2, 31, v7
	v_and_b32_e32 v2, 0x7fffff80, v2
	v_and_b32_e32 v3, 0xffffff80, v7
	v_bitop3_b32 v2, v2, v127, v3 bitop3:0xde
	ds_write2_b32 v39, v23, v2 offset0:136 offset1:168
	v_ashrrev_i32_e32 v2, 31, v8
	v_and_b32_e32 v2, 0x7fffff80, v2
	v_and_b32_e32 v3, 0xffffff80, v8
	v_bitop3_b32 v2, v2, v127, v3 bitop3:0xde
	ds_write2_b32 v40, v24, v2 offset0:144 offset1:176
	v_ashrrev_i32_e32 v2, 31, v9
	v_and_b32_e32 v2, 0x7fffff80, v2
	v_and_b32_e32 v3, 0xffffff80, v9
	v_bitop3_b32 v2, v2, v127, v3 bitop3:0xde
	ds_write2_b32 v41, v25, v2 offset0:152 offset1:184
	v_ashrrev_i32_e32 v2, 31, v10
	v_and_b32_e32 v2, 0x7fffff80, v2
	v_and_b32_e32 v3, 0xffffff80, v10
	v_bitop3_b32 v2, v2, v127, v3 bitop3:0xde
	ds_write2_b32 v128, v26, v2 offset0:64 offset1:96
	v_ashrrev_i32_e32 v2, 31, v11
	v_and_b32_e32 v2, 0x7fffff80, v2
	v_and_b32_e32 v3, 0xffffff80, v11
	v_bitop3_b32 v2, v2, v127, v3 bitop3:0xde
	ds_write2_b32 v129, v27, v2 offset0:64 offset1:96
	v_ashrrev_i32_e32 v2, 31, v12
	v_and_b32_e32 v2, 0x7fffff80, v2
	v_and_b32_e32 v3, 0xffffff80, v12
	v_bitop3_b32 v2, v2, v127, v3 bitop3:0xde
	ds_write2_b32 v130, v28, v2 offset0:64 offset1:96
	v_ashrrev_i32_e32 v2, 31, v13
	v_and_b32_e32 v2, 0x7fffff80, v2
	v_and_b32_e32 v3, 0xffffff80, v13
	v_bitop3_b32 v2, v2, v127, v3 bitop3:0xde
	ds_write2_b32 v131, v29, v2 offset0:64 offset1:96
	v_ashrrev_i32_e32 v2, 31, v14
	v_and_b32_e32 v2, 0x7fffff80, v2
	v_and_b32_e32 v3, 0xffffff80, v14
	v_bitop3_b32 v2, v2, v127, v3 bitop3:0xde
	ds_write2_b32 v132, v30, v2 offset0:64 offset1:96
	v_ashrrev_i32_e32 v2, 31, v15
	v_and_b32_e32 v2, 0x7fffff80, v2
	v_and_b32_e32 v3, 0xffffff80, v15
	v_bitop3_b32 v2, v2, v127, v3 bitop3:0xde
	ds_write2_b32 v133, v31, v2 offset0:64 offset1:96
	v_ashrrev_i32_e32 v2, 31, v16
	v_and_b32_e32 v2, 0x7fffff80, v2
	v_and_b32_e32 v3, 0xffffff80, v16
	v_bitop3_b32 v2, v2, v127, v3 bitop3:0xde
	ds_write2_b32 v134, v32, v2 offset0:64 offset1:96
	v_ashrrev_i32_e32 v2, 31, v17
	v_and_b32_e32 v2, 0x7fffff80, v2
	v_and_b32_e32 v3, 0xffffff80, v17
	v_bitop3_b32 v2, v2, v127, v3 bitop3:0xde
	ds_write2_b32 v135, v33, v2 offset0:64 offset1:96
	s_waitcnt lgkmcnt(0)
	s_barrier
; #define LAS __attribute__((address_space(3)))
; #define TOPK_INSERT(arr, xx) do { int _x = (xx); _Pragma("unroll") for (int _j = 0; _j < 16; ++_j) { const int _hi = max(arr[_j], _x); _x = min(arr[_j], _x); arr[_j] = _hi; } } while (0)
; DI void routing_block(LAS unsigned char* lds, const bf16* q, const bf16* skb, int* experts, float* pgates, int tb) {
;     ...
;             int a[16];
; #pragma unroll
;             for (int j = 0; j < 16; ++j) a[j] = (int)0x80000000;
;             LAS int* row = sc + (tid >> 1) * RT_PITCH; const int hf = tid & 1;
; #pragma unroll 8
;             for (int k = 0; k < 64; ++k) { const int x = row[64 * hf + k]; TOPK_INSERT(a, x); }
	v_and_b32_e32 v34, 1, v118
	v_lshlrev_b32_e32 v34, 7, v34
	v_sub_u32_e32 v35, v120, v34
	v_add_u32_e32 v34, v120, v34
	ds_read2_b32 v[146:147], v34 offset0:0 offset1:1
	ds_read2_b32 v[148:149], v34 offset0:2 offset1:3
	ds_read2_b32 v[150:151], v34 offset0:4 offset1:5
	ds_read2_b32 v[152:153], v34 offset0:6 offset1:7
	ds_read2_b32 v[154:155], v34 offset0:8 offset1:9
	ds_read2_b32 v[156:157], v34 offset0:10 offset1:11
	ds_read2_b32 v[158:159], v34 offset0:12 offset1:13
	ds_read2_b32 v[160:161], v34 offset0:14 offset1:15
	ds_read2_b32 v[162:163], v34 offset0:16 offset1:17
	ds_read2_b32 v[164:165], v34 offset0:18 offset1:19
	ds_read2_b32 v[166:167], v34 offset0:20 offset1:21
	ds_read2_b32 v[168:169], v34 offset0:22 offset1:23
	ds_read2_b32 v[170:171], v34 offset0:24 offset1:25
	ds_read2_b32 v[172:173], v34 offset0:26 offset1:27
	ds_read2_b32 v[174:175], v34 offset0:28 offset1:29
	ds_read2_b32 v[176:177], v34 offset0:30 offset1:31
	ds_read2_b32 v[178:179], v35 offset0:32 offset1:33
	ds_read2_b32 v[180:181], v35 offset0:34 offset1:35
	ds_read2_b32 v[182:183], v35 offset0:36 offset1:37
	ds_read2_b32 v[184:185], v35 offset0:38 offset1:39
	ds_read2_b32 v[186:187], v35 offset0:40 offset1:41
	ds_read2_b32 v[188:189], v35 offset0:42 offset1:43
	ds_read2_b32 v[190:191], v35 offset0:44 offset1:45
	ds_read2_b32 v[192:193], v35 offset0:46 offset1:47
	ds_read2_b32 v[194:195], v35 offset0:48 offset1:49
	ds_read2_b32 v[196:197], v35 offset0:50 offset1:51
	ds_read2_b32 v[198:199], v35 offset0:52 offset1:53
	ds_read2_b32 v[200:201], v35 offset0:54 offset1:55
	ds_read2_b32 v[202:203], v35 offset0:56 offset1:57
	ds_read2_b32 v[204:205], v35 offset0:58 offset1:59
	ds_read2_b32 v[206:207], v35 offset0:60 offset1:61
	ds_read2_b32 v[208:209], v35 offset0:62 offset1:63
	s_waitcnt lgkmcnt(15)
	v_max_i32_e32 v18, v146, v147
	v_min_i32_e32 v147, v146, v147
	v_max_i32_e32 v19, v148, v149
	v_min_i32_e32 v149, v148, v149
	v_max_i32_e32 v20, v18, v19
	v_min_i32_e32 v19, v18, v19
	v_max_i32_e32 v21, v147, v149
	v_min_i32_e32 v149, v147, v149
	v_max_i32_e32 v146, v21, v19
	v_min_i32_e32 v19, v21, v19
	v_max_i32_e32 v148, v150, v151
	v_min_i32_e32 v151, v150, v151
	v_max_i32_e32 v18, v152, v153
	v_min_i32_e32 v153, v152, v153
	v_max_i32_e32 v147, v148, v18
	v_min_i32_e32 v18, v148, v18
	v_max_i32_e32 v21, v151, v153
	v_min_i32_e32 v153, v151, v153
	v_max_i32_e32 v150, v21, v18
	v_min_i32_e32 v18, v21, v18
	v_max_i32_e32 v152, v20, v147
	v_min_i32_e32 v147, v20, v147
	v_max_i32_e32 v148, v19, v18
	v_min_i32_e32 v18, v19, v18
	v_max_i32_e32 v151, v148, v147
	v_min_i32_e32 v147, v148, v147
	v_max_i32_e32 v21, v146, v150
	v_min_i32_e32 v150, v146, v150
	v_max_i32_e32 v20, v149, v153
	v_min_i32_e32 v153, v149, v153
	v_max_i32_e32 v19, v20, v150
	v_min_i32_e32 v150, v20, v150
	v_max_i32_e32 v148, v21, v151
	v_min_i32_e32 v151, v21, v151
	v_max_i32_e32 v146, v19, v147
	v_min_i32_e32 v147, v19, v147
	v_max_i32_e32 v149, v150, v18
	v_min_i32_e32 v18, v150, v18
	v_max_i32_e32 v20, v154, v155
	v_min_i32_e32 v155, v154, v155
	v_max_i32_e32 v21, v156, v157
	v_min_i32_e32 v157, v156, v157
	v_max_i32_e32 v19, v20, v21
	v_min_i32_e32 v21, v20, v21
	v_max_i32_e32 v150, v155, v157
	v_min_i32_e32 v157, v155, v157
	v_max_i32_e32 v154, v150, v21
	v_min_i32_e32 v21, v150, v21
	v_max_i32_e32 v156, v158, v159
	v_min_i32_e32 v159, v158, v159
	v_max_i32_e32 v20, v160, v161
	v_min_i32_e32 v161, v160, v161
	v_max_i32_e32 v155, v156, v20
	v_min_i32_e32 v20, v156, v20
	v_max_i32_e32 v150, v159, v161
	v_min_i32_e32 v161, v159, v161
	v_max_i32_e32 v158, v150, v20
	v_min_i32_e32 v20, v150, v20
	v_max_i32_e32 v160, v19, v155
	v_min_i32_e32 v155, v19, v155
	v_max_i32_e32 v156, v21, v20
	v_min_i32_e32 v20, v21, v20
	v_max_i32_e32 v159, v156, v155
	v_min_i32_e32 v155, v156, v155
	v_max_i32_e32 v150, v154, v158
	v_min_i32_e32 v158, v154, v158
	v_max_i32_e32 v19, v157, v161
	v_min_i32_e32 v161, v157, v161
	v_max_i32_e32 v21, v19, v158
	v_min_i32_e32 v158, v19, v158
	v_max_i32_e32 v156, v150, v159
	v_min_i32_e32 v159, v150, v159
	v_max_i32_e32 v154, v21, v155
	v_min_i32_e32 v155, v21, v155
	v_max_i32_e32 v157, v158, v20
	v_min_i32_e32 v20, v158, v20
	v_max_i32_e32 v19, v152, v160
	v_min_i32_e32 v160, v152, v160
	v_max_i32_e32 v150, v147, v155
	v_min_i32_e32 v155, v147, v155
	v_max_i32_e32 v21, v150, v160
	v_min_i32_e32 v160, v150, v160
	v_max_i32_e32 v158, v151, v159
	v_min_i32_e32 v159, v151, v159
	v_max_i32_e32 v152, v18, v20
	v_min_i32_e32 v20, v18, v20
	v_max_i32_e32 v147, v152, v159
	v_min_i32_e32 v159, v152, v159
	v_max_i32_e32 v150, v158, v21
	v_min_i32_e32 v21, v158, v21
	v_max_i32_e32 v151, v147, v160
	v_min_i32_e32 v160, v147, v160
	v_max_i32_e32 v18, v159, v155
	v_min_i32_e32 v155, v159, v155
	v_max_i32_e32 v152, v148, v156
	v_min_i32_e32 v156, v148, v156
	v_max_i32_e32 v158, v149, v157
	v_min_i32_e32 v157, v149, v157
	v_max_i32_e32 v147, v158, v156
	v_min_i32_e32 v156, v158, v156
	v_max_i32_e32 v159, v146, v154
	v_min_i32_e32 v154, v146, v154
	v_max_i32_e32 v148, v153, v161
	v_min_i32_e32 v161, v153, v161
	v_max_i32_e32 v149, v148, v154
	v_min_i32_e32 v154, v148, v154
	v_max_i32_e32 v158, v159, v147
	v_min_i32_e32 v147, v159, v147
	v_max_i32_e32 v146, v149, v156
	v_min_i32_e32 v156, v149, v156
	v_max_i32_e32 v153, v154, v157
	v_min_i32_e32 v157, v154, v157
	v_max_i32_e32 v148, v152, v150
	v_min_i32_e32 v150, v152, v150
	v_max_i32_e32 v159, v158, v21
	v_min_i32_e32 v21, v158, v21
	v_max_i32_e32 v149, v147, v151
	v_min_i32_e32 v151, v147, v151
	v_max_i32_e32 v154, v146, v160
	v_min_i32_e32 v160, v146, v160
	v_max_i32_e32 v152, v156, v18
	v_min_i32_e32 v18, v156, v18
	v_max_i32_e32 v158, v153, v155
	v_min_i32_e32 v155, v153, v155
	v_max_i32_e32 v147, v157, v20
	v_min_i32_e32 v20, v157, v20
	s_waitcnt lgkmcnt(15)
; #define TOPK_INSERT(arr, xx) do { int _x = (xx); _Pragma("unroll") for (int _j = 0; _j < 16; ++_j) { const int _hi = max(arr[_j], _x); _x = min(arr[_j], _x); arr[_j] = _hi; } } while (0)
; DI void routing_block(LAS unsigned char* lds, const bf16* q, const bf16* skb, int* experts, float* pgates, int tb) {
;     ...
;             for (int k = 0; k < 64; ++k) { const int x = row[64 * hf + k]; TOPK_INSERT(a, x); }
	v_max_i32_e32 v146, v162, v163
	v_min_i32_e32 v163, v162, v163
	v_max_i32_e32 v156, v164, v165
	v_min_i32_e32 v165, v164, v165
	v_max_i32_e32 v153, v146, v156
	v_min_i32_e32 v156, v146, v156
	v_max_i32_e32 v157, v163, v165
	v_min_i32_e32 v165, v163, v165
	v_max_i32_e32 v162, v157, v156
	v_min_i32_e32 v156, v157, v156
	v_max_i32_e32 v164, v166, v167
	v_min_i32_e32 v167, v166, v167
	v_max_i32_e32 v146, v168, v169
	v_min_i32_e32 v169, v168, v169
	v_max_i32_e32 v163, v164, v146
	v_min_i32_e32 v146, v164, v146
	v_max_i32_e32 v157, v167, v169
	v_min_i32_e32 v169, v167, v169
	v_max_i32_e32 v166, v157, v146
	v_min_i32_e32 v146, v157, v146
	v_max_i32_e32 v168, v153, v163
	v_min_i32_e32 v163, v153, v163
	v_max_i32_e32 v164, v156, v146
	v_min_i32_e32 v146, v156, v146
	v_max_i32_e32 v167, v164, v163
	v_min_i32_e32 v163, v164, v163
	v_max_i32_e32 v157, v162, v166
	v_min_i32_e32 v166, v162, v166
	v_max_i32_e32 v153, v165, v169
	v_min_i32_e32 v169, v165, v169
	v_max_i32_e32 v156, v153, v166
	v_min_i32_e32 v166, v153, v166
	v_max_i32_e32 v164, v157, v167
	v_min_i32_e32 v167, v157, v167
	v_max_i32_e32 v162, v156, v163
	v_min_i32_e32 v163, v156, v163
	v_max_i32_e32 v165, v166, v146
	v_min_i32_e32 v146, v166, v146
	v_max_i32_e32 v153, v170, v171
	v_min_i32_e32 v171, v170, v171
	v_max_i32_e32 v157, v172, v173
	v_min_i32_e32 v173, v172, v173
	v_max_i32_e32 v156, v153, v157
	v_min_i32_e32 v157, v153, v157
	v_max_i32_e32 v166, v171, v173
	v_min_i32_e32 v173, v171, v173
	v_max_i32_e32 v170, v166, v157
	v_min_i32_e32 v157, v166, v157
	v_max_i32_e32 v172, v174, v175
	v_min_i32_e32 v175, v174, v175
	v_max_i32_e32 v153, v176, v177
	v_min_i32_e32 v177, v176, v177
	v_max_i32_e32 v171, v172, v153
	v_min_i32_e32 v153, v172, v153
	v_max_i32_e32 v166, v175, v177
	v_min_i32_e32 v177, v175, v177
	v_max_i32_e32 v174, v166, v153
	v_min_i32_e32 v153, v166, v153
	v_max_i32_e32 v176, v156, v171
	v_min_i32_e32 v171, v156, v171
	v_max_i32_e32 v172, v157, v153
	v_min_i32_e32 v153, v157, v153
	v_max_i32_e32 v175, v172, v171
	v_min_i32_e32 v171, v172, v171
	v_max_i32_e32 v166, v170, v174
	v_min_i32_e32 v174, v170, v174
	v_max_i32_e32 v156, v173, v177
	v_min_i32_e32 v177, v173, v177
	v_max_i32_e32 v157, v156, v174
	v_min_i32_e32 v174, v156, v174
	v_max_i32_e32 v172, v166, v175
	v_min_i32_e32 v175, v166, v175
	v_max_i32_e32 v170, v157, v171
	v_min_i32_e32 v171, v157, v171
	v_max_i32_e32 v173, v174, v153
	v_min_i32_e32 v153, v174, v153
	v_max_i32_e32 v156, v168, v176
	v_min_i32_e32 v176, v168, v176
	v_max_i32_e32 v166, v163, v171
	v_min_i32_e32 v171, v163, v171
	v_max_i32_e32 v157, v166, v176
	v_min_i32_e32 v176, v166, v176
	v_max_i32_e32 v174, v167, v175
	v_min_i32_e32 v175, v167, v175
	v_max_i32_e32 v168, v146, v153
	v_min_i32_e32 v153, v146, v153
	v_max_i32_e32 v163, v168, v175
	v_min_i32_e32 v175, v168, v175
	v_max_i32_e32 v166, v174, v157
	v_min_i32_e32 v157, v174, v157
	v_max_i32_e32 v167, v163, v176
	v_min_i32_e32 v176, v163, v176
	v_max_i32_e32 v146, v175, v171
	v_min_i32_e32 v171, v175, v171
	v_max_i32_e32 v168, v164, v172
	v_min_i32_e32 v172, v164, v172
	v_max_i32_e32 v174, v165, v173
	v_min_i32_e32 v173, v165, v173
	v_max_i32_e32 v163, v174, v172
	v_min_i32_e32 v172, v174, v172
	v_max_i32_e32 v175, v162, v170
	v_min_i32_e32 v170, v162, v170
	v_max_i32_e32 v164, v169, v177
	v_min_i32_e32 v177, v169, v177
	v_max_i32_e32 v165, v164, v170
	v_min_i32_e32 v170, v164, v170
	v_max_i32_e32 v174, v175, v163
	v_min_i32_e32 v163, v175, v163
	v_max_i32_e32 v162, v165, v172
	v_min_i32_e32 v172, v165, v172
	v_max_i32_e32 v169, v170, v173
	v_min_i32_e32 v173, v170, v173
	v_max_i32_e32 v164, v168, v166
	v_min_i32_e32 v166, v168, v166
	v_max_i32_e32 v175, v174, v157
	v_min_i32_e32 v157, v174, v157
	v_max_i32_e32 v165, v163, v167
	v_min_i32_e32 v167, v163, v167
	v_max_i32_e32 v170, v162, v176
	v_min_i32_e32 v176, v162, v176
	v_max_i32_e32 v168, v172, v146
	v_min_i32_e32 v146, v172, v146
	v_max_i32_e32 v174, v169, v171
	v_min_i32_e32 v171, v169, v171
	v_max_i32_e32 v163, v173, v153
	v_min_i32_e32 v153, v173, v153
	s_waitcnt lgkmcnt(8)
	v_max_i32_e32 v162, v178, v179
	v_min_i32_e32 v179, v178, v179
	v_max_i32_e32 v172, v180, v181
	v_min_i32_e32 v181, v180, v181
	v_max_i32_e32 v169, v162, v172
	v_min_i32_e32 v172, v162, v172
	v_max_i32_e32 v173, v179, v181
	v_min_i32_e32 v181, v179, v181
	v_max_i32_e32 v178, v173, v172
	v_min_i32_e32 v172, v173, v172
	v_max_i32_e32 v180, v182, v183
	v_min_i32_e32 v183, v182, v183
	v_max_i32_e32 v162, v184, v185
	v_min_i32_e32 v185, v184, v185
	v_max_i32_e32 v179, v180, v162
	v_min_i32_e32 v162, v180, v162
	v_max_i32_e32 v173, v183, v185
	v_min_i32_e32 v185, v183, v185
	v_max_i32_e32 v182, v173, v162
	v_min_i32_e32 v162, v173, v162
	v_max_i32_e32 v184, v169, v179
	v_min_i32_e32 v179, v169, v179
	v_max_i32_e32 v180, v172, v162
	v_min_i32_e32 v162, v172, v162
	v_max_i32_e32 v183, v180, v179
	v_min_i32_e32 v179, v180, v179
	v_max_i32_e32 v173, v178, v182
	v_min_i32_e32 v182, v178, v182
	v_max_i32_e32 v169, v181, v185
	v_min_i32_e32 v185, v181, v185
	v_max_i32_e32 v172, v169, v182
	v_min_i32_e32 v182, v169, v182
	v_max_i32_e32 v180, v173, v183
	v_min_i32_e32 v183, v173, v183
	v_max_i32_e32 v178, v172, v179
	v_min_i32_e32 v179, v172, v179
	v_max_i32_e32 v181, v182, v162
	v_min_i32_e32 v162, v182, v162
	v_max_i32_e32 v169, v186, v187
	v_min_i32_e32 v187, v186, v187
	v_max_i32_e32 v173, v188, v189
	v_min_i32_e32 v189, v188, v189
	v_max_i32_e32 v172, v169, v173
	v_min_i32_e32 v173, v169, v173
	v_max_i32_e32 v182, v187, v189
	v_min_i32_e32 v189, v187, v189
	v_max_i32_e32 v186, v182, v173
	v_min_i32_e32 v173, v182, v173
	v_max_i32_e32 v188, v190, v191
	v_min_i32_e32 v191, v190, v191
; #define TOPK_INSERT(arr, xx) do { int _x = (xx); _Pragma("unroll") for (int _j = 0; _j < 16; ++_j) { const int _hi = max(arr[_j], _x); _x = min(arr[_j], _x); arr[_j] = _hi; } } while (0)
; DI void routing_block(LAS unsigned char* lds, const bf16* q, const bf16* skb, int* experts, float* pgates, int tb) {
;     ...
;             for (int k = 0; k < 64; ++k) { const int x = row[64 * hf + k]; TOPK_INSERT(a, x); }
	v_max_i32_e32 v169, v192, v193
	v_min_i32_e32 v193, v192, v193
	v_max_i32_e32 v187, v188, v169
	v_min_i32_e32 v169, v188, v169
	v_max_i32_e32 v182, v191, v193
	v_min_i32_e32 v193, v191, v193
	v_max_i32_e32 v190, v182, v169
	v_min_i32_e32 v169, v182, v169
	v_max_i32_e32 v192, v172, v187
	v_min_i32_e32 v187, v172, v187
	v_max_i32_e32 v188, v173, v169
	v_min_i32_e32 v169, v173, v169
	v_max_i32_e32 v191, v188, v187
	v_min_i32_e32 v187, v188, v187
	v_max_i32_e32 v182, v186, v190
	v_min_i32_e32 v190, v186, v190
	v_max_i32_e32 v172, v189, v193
	v_min_i32_e32 v193, v189, v193
	v_max_i32_e32 v173, v172, v190
	v_min_i32_e32 v190, v172, v190
	v_max_i32_e32 v188, v182, v191
	v_min_i32_e32 v191, v182, v191
	v_max_i32_e32 v186, v173, v187
	v_min_i32_e32 v187, v173, v187
	v_max_i32_e32 v189, v190, v169
	v_min_i32_e32 v169, v190, v169
	v_max_i32_e32 v172, v184, v192
	v_min_i32_e32 v192, v184, v192
	v_max_i32_e32 v182, v179, v187
	v_min_i32_e32 v187, v179, v187
	v_max_i32_e32 v173, v182, v192
	v_min_i32_e32 v192, v182, v192
	v_max_i32_e32 v190, v183, v191
	v_min_i32_e32 v191, v183, v191
	v_max_i32_e32 v184, v162, v169
	v_min_i32_e32 v169, v162, v169
	v_max_i32_e32 v179, v184, v191
	v_min_i32_e32 v191, v184, v191
	v_max_i32_e32 v182, v190, v173
	v_min_i32_e32 v173, v190, v173
	v_max_i32_e32 v183, v179, v192
	v_min_i32_e32 v192, v179, v192
	v_max_i32_e32 v162, v191, v187
	v_min_i32_e32 v187, v191, v187
	v_max_i32_e32 v184, v180, v188
	v_min_i32_e32 v188, v180, v188
	v_max_i32_e32 v190, v181, v189
	v_min_i32_e32 v189, v181, v189
	v_max_i32_e32 v179, v190, v188
	v_min_i32_e32 v188, v190, v188
	v_max_i32_e32 v191, v178, v186
	v_min_i32_e32 v186, v178, v186
	v_max_i32_e32 v180, v185, v193
	v_min_i32_e32 v193, v185, v193
	v_max_i32_e32 v181, v180, v186
	v_min_i32_e32 v186, v180, v186
	v_max_i32_e32 v190, v191, v179
	v_min_i32_e32 v179, v191, v179
	v_max_i32_e32 v178, v181, v188
	v_min_i32_e32 v188, v181, v188
	v_max_i32_e32 v185, v186, v189
	v_min_i32_e32 v189, v186, v189
	v_max_i32_e32 v180, v184, v182
	v_min_i32_e32 v182, v184, v182
	v_max_i32_e32 v191, v190, v173
	v_min_i32_e32 v173, v190, v173
	v_max_i32_e32 v181, v179, v183
	v_min_i32_e32 v183, v179, v183
	v_max_i32_e32 v186, v178, v192
	v_min_i32_e32 v192, v178, v192
	v_max_i32_e32 v184, v188, v162
	v_min_i32_e32 v162, v188, v162
	v_max_i32_e32 v190, v185, v187
	v_min_i32_e32 v187, v185, v187
	v_max_i32_e32 v179, v189, v169
	v_min_i32_e32 v169, v189, v169
	s_waitcnt lgkmcnt(0)
	v_max_i32_e32 v178, v194, v195
	v_min_i32_e32 v195, v194, v195
	v_max_i32_e32 v188, v196, v197
	v_min_i32_e32 v197, v196, v197
	v_max_i32_e32 v185, v178, v188
	v_min_i32_e32 v188, v178, v188
	v_max_i32_e32 v189, v195, v197
	v_min_i32_e32 v197, v195, v197
	v_max_i32_e32 v194, v189, v188
	v_min_i32_e32 v188, v189, v188
	v_max_i32_e32 v196, v198, v199
	v_min_i32_e32 v199, v198, v199
	v_max_i32_e32 v178, v200, v201
	v_min_i32_e32 v201, v200, v201
	v_max_i32_e32 v195, v196, v178
	v_min_i32_e32 v178, v196, v178
	v_max_i32_e32 v189, v199, v201
	v_min_i32_e32 v201, v199, v201
	v_max_i32_e32 v198, v189, v178
	v_min_i32_e32 v178, v189, v178
	v_max_i32_e32 v200, v185, v195
	v_min_i32_e32 v195, v185, v195
	v_max_i32_e32 v196, v188, v178
	v_min_i32_e32 v178, v188, v178
	v_max_i32_e32 v199, v196, v195
	v_min_i32_e32 v195, v196, v195
	v_max_i32_e32 v189, v194, v198
	v_min_i32_e32 v198, v194, v198
	v_max_i32_e32 v185, v197, v201
	v_min_i32_e32 v201, v197, v201
	v_max_i32_e32 v188, v185, v198
	v_min_i32_e32 v198, v185, v198
	v_max_i32_e32 v196, v189, v199
	v_min_i32_e32 v199, v189, v199
	v_max_i32_e32 v194, v188, v195
	v_min_i32_e32 v195, v188, v195
	v_max_i32_e32 v197, v198, v178
	v_min_i32_e32 v178, v198, v178
	v_max_i32_e32 v185, v202, v203
	v_min_i32_e32 v203, v202, v203
	v_max_i32_e32 v189, v204, v205
	v_min_i32_e32 v205, v204, v205
	v_max_i32_e32 v188, v185, v189
	v_min_i32_e32 v189, v185, v189
	v_max_i32_e32 v198, v203, v205
	v_min_i32_e32 v205, v203, v205
	v_max_i32_e32 v202, v198, v189
	v_min_i32_e32 v189, v198, v189
	v_max_i32_e32 v204, v206, v207
	v_min_i32_e32 v207, v206, v207
	v_max_i32_e32 v185, v208, v209
	v_min_i32_e32 v209, v208, v209
	v_max_i32_e32 v203, v204, v185
	v_min_i32_e32 v185, v204, v185
	v_max_i32_e32 v198, v207, v209
	v_min_i32_e32 v209, v207, v209
	v_max_i32_e32 v206, v198, v185
	v_min_i32_e32 v185, v198, v185
	v_max_i32_e32 v208, v188, v203
	v_min_i32_e32 v203, v188, v203
	v_max_i32_e32 v204, v189, v185
	v_min_i32_e32 v185, v189, v185
	v_max_i32_e32 v207, v204, v203
	v_min_i32_e32 v203, v204, v203
	v_max_i32_e32 v198, v202, v206
	v_min_i32_e32 v206, v202, v206
	v_max_i32_e32 v188, v205, v209
	v_min_i32_e32 v209, v205, v209
	v_max_i32_e32 v189, v188, v206
	v_min_i32_e32 v206, v188, v206
	v_max_i32_e32 v204, v198, v207
	v_min_i32_e32 v207, v198, v207
	v_max_i32_e32 v202, v189, v203
	v_min_i32_e32 v203, v189, v203
	v_max_i32_e32 v205, v206, v185
	v_min_i32_e32 v185, v206, v185
	v_max_i32_e32 v188, v200, v208
	v_min_i32_e32 v208, v200, v208
	v_max_i32_e32 v198, v195, v203
	v_min_i32_e32 v203, v195, v203
	v_max_i32_e32 v189, v198, v208
	v_min_i32_e32 v208, v198, v208
	v_max_i32_e32 v206, v199, v207
	v_min_i32_e32 v207, v199, v207
	v_max_i32_e32 v200, v178, v185
	v_min_i32_e32 v185, v178, v185
	v_max_i32_e32 v195, v200, v207
	v_min_i32_e32 v207, v200, v207
	v_max_i32_e32 v198, v206, v189
	v_min_i32_e32 v189, v206, v189
	v_max_i32_e32 v199, v195, v208
	v_min_i32_e32 v208, v195, v208
	v_max_i32_e32 v178, v207, v203
	v_min_i32_e32 v203, v207, v203
	v_max_i32_e32 v200, v196, v204
	v_min_i32_e32 v204, v196, v204
	v_max_i32_e32 v206, v197, v205
	v_min_i32_e32 v205, v197, v205
	v_max_i32_e32 v195, v206, v204
	v_min_i32_e32 v204, v206, v204
; #define TOPK_INSERT(arr, xx) do { int _x = (xx); _Pragma("unroll") for (int _j = 0; _j < 16; ++_j) { const int _hi = max(arr[_j], _x); _x = min(arr[_j], _x); arr[_j] = _hi; } } while (0)
; DI void routing_block(LAS unsigned char* lds, const bf16* q, const bf16* skb, int* experts, float* pgates, int tb) {
;     ...
;             for (int k = 0; k < 64; ++k) { const int x = row[64 * hf + k]; TOPK_INSERT(a, x); }
;             __syncthreads();
; #pragma unroll
;             for (int j = 0; j < 16; ++j) row[16 * hf + j] = a[j];
;             __syncthreads();
;             if (hf == 0) {
; #pragma unroll
;                 for (int j = 0; j < 16; ++j) { const int x = row[16 + j]; TOPK_INSERT(a, x); }
	v_max_i32_e32 v207, v194, v202
	v_min_i32_e32 v202, v194, v202
	v_max_i32_e32 v196, v201, v209
	v_min_i32_e32 v209, v201, v209
	v_max_i32_e32 v197, v196, v202
	v_min_i32_e32 v202, v196, v202
	v_max_i32_e32 v206, v207, v195
	v_min_i32_e32 v195, v207, v195
	v_max_i32_e32 v194, v197, v204
	v_min_i32_e32 v204, v197, v204
	v_max_i32_e32 v201, v202, v205
	v_min_i32_e32 v205, v202, v205
	v_max_i32_e32 v196, v200, v198
	v_min_i32_e32 v198, v200, v198
	v_max_i32_e32 v207, v206, v189
	v_min_i32_e32 v189, v206, v189
	v_max_i32_e32 v197, v195, v199
	v_min_i32_e32 v199, v195, v199
	v_max_i32_e32 v202, v194, v208
	v_min_i32_e32 v208, v194, v208
	v_max_i32_e32 v200, v204, v178
	v_min_i32_e32 v178, v204, v178
	v_max_i32_e32 v206, v201, v203
	v_min_i32_e32 v203, v201, v203
	v_max_i32_e32 v195, v205, v185
	v_min_i32_e32 v185, v205, v185
	v_max_i32_e32 v19, v19, v177
	v_max_i32_e32 v148, v148, v153
	v_max_i32_e32 v150, v150, v163
	v_max_i32_e32 v159, v159, v171
	v_max_i32_e32 v21, v21, v174
	v_max_i32_e32 v149, v149, v146
	v_max_i32_e32 v151, v151, v168
	v_max_i32_e32 v154, v154, v176
	v_max_i32_e32 v160, v160, v170
	v_max_i32_e32 v152, v152, v167
	v_max_i32_e32 v18, v18, v165
	v_max_i32_e32 v158, v158, v157
	v_max_i32_e32 v155, v155, v175
	v_max_i32_e32 v147, v147, v166
	v_max_i32_e32 v20, v20, v164
	v_max_i32_e32 v161, v161, v156
	v_max_i32_e32 v194, v19, v160
	v_min_i32_e32 v160, v19, v160
	v_max_i32_e32 v204, v148, v152
	v_min_i32_e32 v152, v148, v152
	v_max_i32_e32 v201, v150, v18
	v_min_i32_e32 v18, v150, v18
	v_max_i32_e32 v205, v159, v158
	v_min_i32_e32 v158, v159, v158
	v_max_i32_e32 v156, v21, v155
	v_min_i32_e32 v155, v21, v155
	v_max_i32_e32 v164, v149, v147
	v_min_i32_e32 v147, v149, v147
	v_max_i32_e32 v166, v151, v20
	v_min_i32_e32 v20, v151, v20
	v_max_i32_e32 v175, v154, v161
	v_min_i32_e32 v161, v154, v161
	v_max_i32_e32 v157, v194, v156
	v_min_i32_e32 v156, v194, v156
	v_max_i32_e32 v165, v204, v164
	v_min_i32_e32 v164, v204, v164
	v_max_i32_e32 v167, v201, v166
	v_min_i32_e32 v166, v201, v166
	v_max_i32_e32 v170, v205, v175
	v_min_i32_e32 v175, v205, v175
	v_max_i32_e32 v176, v160, v155
	v_min_i32_e32 v155, v160, v155
	v_max_i32_e32 v168, v152, v147
	v_min_i32_e32 v147, v152, v147
	v_max_i32_e32 v146, v18, v20
	v_min_i32_e32 v20, v18, v20
	v_max_i32_e32 v174, v158, v161
	v_min_i32_e32 v161, v158, v161
	v_max_i32_e32 v171, v157, v167
	v_min_i32_e32 v167, v157, v167
	v_max_i32_e32 v163, v165, v170
	v_min_i32_e32 v170, v165, v170
	v_max_i32_e32 v153, v156, v166
	v_min_i32_e32 v166, v156, v166
	v_max_i32_e32 v177, v164, v175
	v_min_i32_e32 v175, v164, v175
	v_max_i32_e32 v19, v176, v146
	v_min_i32_e32 v146, v176, v146
	v_max_i32_e32 v148, v168, v174
	v_min_i32_e32 v174, v168, v174
	v_max_i32_e32 v150, v155, v20
	v_min_i32_e32 v20, v155, v20
	v_max_i32_e32 v159, v147, v161
	v_min_i32_e32 v161, v147, v161
	v_max_i32_e32 v21, v171, v163
	v_min_i32_e32 v163, v171, v163
	v_max_i32_e32 v149, v167, v170
	v_min_i32_e32 v170, v167, v170
	v_max_i32_e32 v151, v153, v177
	v_min_i32_e32 v177, v153, v177
	v_max_i32_e32 v154, v166, v175
	v_min_i32_e32 v175, v166, v175
	v_max_i32_e32 v194, v19, v148
	v_min_i32_e32 v148, v19, v148
	v_max_i32_e32 v204, v146, v174
	v_min_i32_e32 v174, v146, v174
	v_max_i32_e32 v201, v150, v159
	v_min_i32_e32 v159, v150, v159
	v_max_i32_e32 v205, v20, v161
	v_min_i32_e32 v161, v20, v161
	v_max_i32_e32 v172, v172, v209
	v_max_i32_e32 v180, v180, v185
	v_max_i32_e32 v182, v182, v195
	v_max_i32_e32 v191, v191, v203
	v_max_i32_e32 v173, v173, v206
	v_max_i32_e32 v181, v181, v178
	v_max_i32_e32 v183, v183, v200
	v_max_i32_e32 v186, v186, v208
	v_max_i32_e32 v192, v192, v202
	v_max_i32_e32 v184, v184, v199
	v_max_i32_e32 v162, v162, v197
	v_max_i32_e32 v190, v190, v189
	v_max_i32_e32 v187, v187, v207
	v_max_i32_e32 v179, v179, v198
	v_max_i32_e32 v169, v169, v196
	v_max_i32_e32 v193, v193, v188
	v_max_i32_e32 v160, v172, v192
	v_min_i32_e32 v192, v172, v192
	v_max_i32_e32 v152, v180, v184
	v_min_i32_e32 v184, v180, v184
	v_max_i32_e32 v18, v182, v162
	v_min_i32_e32 v162, v182, v162
	v_max_i32_e32 v158, v191, v190
	v_min_i32_e32 v190, v191, v190
	v_max_i32_e32 v157, v173, v187
	v_min_i32_e32 v187, v173, v187
	v_max_i32_e32 v165, v181, v179
	v_min_i32_e32 v179, v181, v179
	v_max_i32_e32 v156, v183, v169
	v_min_i32_e32 v169, v183, v169
	v_max_i32_e32 v164, v186, v193
	v_min_i32_e32 v193, v186, v193
	v_max_i32_e32 v176, v160, v157
	v_min_i32_e32 v157, v160, v157
	v_max_i32_e32 v168, v152, v165
	v_min_i32_e32 v165, v152, v165
	v_max_i32_e32 v155, v18, v156
	v_min_i32_e32 v156, v18, v156
	v_max_i32_e32 v147, v158, v164
	v_min_i32_e32 v164, v158, v164
	v_max_i32_e32 v171, v192, v187
	v_min_i32_e32 v187, v192, v187
	v_max_i32_e32 v167, v184, v179
	v_min_i32_e32 v179, v184, v179
	v_max_i32_e32 v153, v162, v169
	v_min_i32_e32 v169, v162, v169
	v_max_i32_e32 v166, v190, v193
	v_min_i32_e32 v193, v190, v193
	v_max_i32_e32 v19, v176, v155
	v_min_i32_e32 v155, v176, v155
	v_max_i32_e32 v146, v168, v147
	v_min_i32_e32 v147, v168, v147
	v_max_i32_e32 v150, v157, v156
	v_min_i32_e32 v156, v157, v156
	v_max_i32_e32 v20, v165, v164
	v_min_i32_e32 v164, v165, v164
	v_max_i32_e32 v188, v171, v153
	v_min_i32_e32 v153, v171, v153
	v_max_i32_e32 v196, v167, v166
	v_min_i32_e32 v166, v167, v166
	v_max_i32_e32 v198, v187, v169
	v_min_i32_e32 v169, v187, v169
	v_max_i32_e32 v207, v179, v193
	v_min_i32_e32 v193, v179, v193
	v_max_i32_e32 v189, v19, v146
	v_min_i32_e32 v146, v19, v146
	v_max_i32_e32 v197, v155, v147
	v_min_i32_e32 v147, v155, v147
	v_max_i32_e32 v199, v150, v20
	v_min_i32_e32 v20, v150, v20
	v_max_i32_e32 v202, v156, v164
	v_min_i32_e32 v164, v156, v164
; #define TOPK_INSERT(arr, xx) do { int _x = (xx); _Pragma("unroll") for (int _j = 0; _j < 16; ++_j) { const int _hi = max(arr[_j], _x); _x = min(arr[_j], _x); arr[_j] = _hi; } } while (0)
; DI void routing_block(LAS unsigned char* lds, const bf16* q, const bf16* skb, int* experts, float* pgates, int tb) {
;     ...
;             __syncthreads();
; #pragma unroll
;             for (int j = 0; j < 16; ++j) row[16 * hf + j] = a[j];
;             __syncthreads();
;             if (hf == 0) {
; #pragma unroll
;                 for (int j = 0; j < 16; ++j) { const int x = row[16 + j]; TOPK_INSERT(a, x); }
; #pragma unroll
;                 for (int j = 0; j < 16; ++j) row[j] = a[j];
;             }
	v_max_i32_e32 v208, v188, v196
	v_min_i32_e32 v196, v188, v196
	v_max_i32_e32 v200, v153, v166
	v_min_i32_e32 v166, v153, v166
	v_max_i32_e32 v178, v198, v207
	v_min_i32_e32 v207, v198, v207
	v_max_i32_e32 v206, v169, v193
	v_min_i32_e32 v193, v169, v193
	v_max_i32_e32 v21, v21, v193
	v_max_i32_e32 v163, v163, v206
	v_max_i32_e32 v149, v149, v207
	v_max_i32_e32 v170, v170, v178
	v_max_i32_e32 v151, v151, v166
	v_max_i32_e32 v177, v177, v200
	v_max_i32_e32 v154, v154, v196
	v_max_i32_e32 v175, v175, v208
	v_max_i32_e32 v194, v194, v164
	v_max_i32_e32 v148, v148, v202
	v_max_i32_e32 v204, v204, v20
	v_max_i32_e32 v174, v174, v199
	v_max_i32_e32 v201, v201, v147
	v_max_i32_e32 v159, v159, v197
	v_max_i32_e32 v205, v205, v146
	v_max_i32_e32 v161, v161, v189
	v_max_i32_e32 v203, v21, v194
	v_min_i32_e32 v194, v21, v194
	v_max_i32_e32 v195, v163, v148
	v_min_i32_e32 v148, v163, v148
	v_max_i32_e32 v185, v149, v204
	v_min_i32_e32 v204, v149, v204
	v_max_i32_e32 v209, v170, v174
	v_min_i32_e32 v174, v170, v174
	v_max_i32_e32 v172, v151, v201
	v_min_i32_e32 v201, v151, v201
	v_max_i32_e32 v180, v177, v159
	v_min_i32_e32 v159, v177, v159
	v_max_i32_e32 v182, v154, v205
	v_min_i32_e32 v205, v154, v205
	v_max_i32_e32 v191, v175, v161
	v_min_i32_e32 v161, v175, v161
	v_max_i32_e32 v173, v203, v172
	v_min_i32_e32 v172, v203, v172
	v_max_i32_e32 v181, v195, v180
	v_min_i32_e32 v180, v195, v180
	v_max_i32_e32 v183, v185, v182
	v_min_i32_e32 v182, v185, v182
	v_max_i32_e32 v186, v209, v191
	v_min_i32_e32 v191, v209, v191
	v_max_i32_e32 v160, v194, v201
	v_min_i32_e32 v201, v194, v201
	v_max_i32_e32 v152, v148, v159
	v_min_i32_e32 v159, v148, v159
	v_max_i32_e32 v18, v204, v205
	v_min_i32_e32 v205, v204, v205
	v_max_i32_e32 v158, v174, v161
	v_min_i32_e32 v161, v174, v161
	v_max_i32_e32 v192, v173, v183
	v_min_i32_e32 v183, v173, v183
	v_max_i32_e32 v184, v181, v186
	v_min_i32_e32 v186, v181, v186
	v_max_i32_e32 v162, v172, v182
	v_min_i32_e32 v182, v172, v182
	v_max_i32_e32 v190, v180, v191
	v_min_i32_e32 v191, v180, v191
	v_max_i32_e32 v176, v160, v18
	v_min_i32_e32 v18, v160, v18
	v_max_i32_e32 v168, v152, v158
	v_min_i32_e32 v158, v152, v158
	v_max_i32_e32 v157, v201, v205
	v_min_i32_e32 v205, v201, v205
	v_max_i32_e32 v165, v159, v161
	v_min_i32_e32 v161, v159, v161
	v_max_i32_e32 v171, v192, v184
	v_min_i32_e32 v184, v192, v184
	v_max_i32_e32 v167, v183, v186
	v_min_i32_e32 v186, v183, v186
	v_max_i32_e32 v187, v162, v190
	v_min_i32_e32 v190, v162, v190
	v_max_i32_e32 v179, v182, v191
	v_min_i32_e32 v191, v182, v191
	v_max_i32_e32 v19, v176, v168
	v_min_i32_e32 v168, v176, v168
	v_max_i32_e32 v155, v18, v158
	v_min_i32_e32 v158, v18, v158
	v_max_i32_e32 v150, v157, v165
	v_min_i32_e32 v165, v157, v165
	v_max_i32_e32 v156, v205, v161
	v_min_i32_e32 v161, v205, v161
	s_nop 1
	v_mov_b32_dpp v34, v171 quad_perm:[1,0,3,2] row_mask:0xf bank_mask:0xf
	v_mov_b32_dpp v35, v184 quad_perm:[1,0,3,2] row_mask:0xf bank_mask:0xf
	v_mov_b32_dpp v36, v167 quad_perm:[1,0,3,2] row_mask:0xf bank_mask:0xf
	v_mov_b32_dpp v37, v186 quad_perm:[1,0,3,2] row_mask:0xf bank_mask:0xf
	v_mov_b32_dpp v38, v187 quad_perm:[1,0,3,2] row_mask:0xf bank_mask:0xf
	v_mov_b32_dpp v39, v190 quad_perm:[1,0,3,2] row_mask:0xf bank_mask:0xf
	v_mov_b32_dpp v40, v179 quad_perm:[1,0,3,2] row_mask:0xf bank_mask:0xf
	v_mov_b32_dpp v41, v191 quad_perm:[1,0,3,2] row_mask:0xf bank_mask:0xf
	v_mov_b32_dpp v42, v19 quad_perm:[1,0,3,2] row_mask:0xf bank_mask:0xf
	v_mov_b32_dpp v43, v168 quad_perm:[1,0,3,2] row_mask:0xf bank_mask:0xf
	v_mov_b32_dpp v44, v155 quad_perm:[1,0,3,2] row_mask:0xf bank_mask:0xf
	v_mov_b32_dpp v45, v158 quad_perm:[1,0,3,2] row_mask:0xf bank_mask:0xf
	v_mov_b32_dpp v46, v150 quad_perm:[1,0,3,2] row_mask:0xf bank_mask:0xf
	v_mov_b32_dpp v47, v165 quad_perm:[1,0,3,2] row_mask:0xf bank_mask:0xf
	v_mov_b32_dpp v48, v156 quad_perm:[1,0,3,2] row_mask:0xf bank_mask:0xf
	v_mov_b32_dpp v49, v161 quad_perm:[1,0,3,2] row_mask:0xf bank_mask:0xf
	v_max_i32_e32 v171, v171, v49
	v_max_i32_e32 v184, v184, v48
	v_max_i32_e32 v167, v167, v47
	v_max_i32_e32 v186, v186, v46
	v_max_i32_e32 v187, v187, v45
	v_max_i32_e32 v190, v190, v44
	v_max_i32_e32 v179, v179, v43
	v_max_i32_e32 v191, v191, v42
	v_max_i32_e32 v19, v19, v41
	v_max_i32_e32 v168, v168, v40
	v_max_i32_e32 v155, v155, v39
	v_max_i32_e32 v158, v158, v38
	v_max_i32_e32 v150, v150, v37
	v_max_i32_e32 v165, v165, v36
	v_max_i32_e32 v156, v156, v35
	v_max_i32_e32 v161, v161, v34
	v_max_i32_e32 v188, v171, v19
	v_min_i32_e32 v19, v171, v19
	v_max_i32_e32 v153, v184, v168
	v_min_i32_e32 v168, v184, v168
	v_max_i32_e32 v198, v167, v155
	v_min_i32_e32 v155, v167, v155
	v_max_i32_e32 v169, v186, v158
	v_min_i32_e32 v158, v186, v158
	v_max_i32_e32 v189, v187, v150
	v_min_i32_e32 v150, v187, v150
	v_max_i32_e32 v146, v190, v165
	v_min_i32_e32 v165, v190, v165
	v_max_i32_e32 v197, v179, v156
	v_min_i32_e32 v156, v179, v156
	v_max_i32_e32 v147, v191, v161
	v_min_i32_e32 v161, v191, v161
	v_max_i32_e32 v199, v188, v189
	v_min_i32_e32 v189, v188, v189
	v_max_i32_e32 v20, v153, v146
	v_min_i32_e32 v146, v153, v146
	v_max_i32_e32 v202, v198, v197
	v_min_i32_e32 v197, v198, v197
	v_max_i32_e32 v164, v169, v147
	v_min_i32_e32 v147, v169, v147
	v_max_i32_e32 v208, v19, v150
	v_min_i32_e32 v150, v19, v150
	v_max_i32_e32 v196, v168, v165
	v_min_i32_e32 v165, v168, v165
	v_max_i32_e32 v200, v155, v156
	v_min_i32_e32 v156, v155, v156
	v_max_i32_e32 v166, v158, v161
	v_min_i32_e32 v161, v158, v161
	v_max_i32_e32 v178, v199, v202
	v_min_i32_e32 v202, v199, v202
	v_max_i32_e32 v207, v20, v164
	v_min_i32_e32 v164, v20, v164
	v_max_i32_e32 v206, v189, v197
	v_min_i32_e32 v197, v189, v197
	v_max_i32_e32 v193, v146, v147
	v_min_i32_e32 v147, v146, v147
	v_max_i32_e32 v21, v208, v200
	v_min_i32_e32 v200, v208, v200
	v_max_i32_e32 v163, v196, v166
	v_min_i32_e32 v166, v196, v166
	v_max_i32_e32 v149, v150, v156
	v_min_i32_e32 v156, v150, v156
	v_max_i32_e32 v170, v165, v161
	v_min_i32_e32 v161, v165, v161
	v_max_i32_e32 v151, v178, v207
	v_min_i32_e32 v207, v178, v207
	v_max_i32_e32 v177, v202, v164
	v_min_i32_e32 v164, v202, v164
	v_max_i32_e32 v154, v206, v193
	v_min_i32_e32 v193, v206, v193
	v_max_i32_e32 v175, v197, v147
	v_min_i32_e32 v147, v197, v147
	v_max_i32_e32 v203, v21, v163
	v_min_i32_e32 v163, v21, v163
	v_max_i32_e32 v195, v200, v166
	v_min_i32_e32 v166, v200, v166
	v_max_i32_e32 v185, v149, v170
	v_min_i32_e32 v170, v149, v170
	v_max_i32_e32 v209, v156, v161
	v_min_i32_e32 v161, v156, v161
	s_and_saveexec_b64 s[76:77], s[44:45]
	s_cbranch_execz .LBB0_898
	ds_write2_b32 v119, v151, v207 offset0:0 offset1:1
	ds_write2_b32 v119, v177, v164 offset0:2 offset1:3
	ds_write2_b32 v119, v154, v193 offset0:4 offset1:5
	ds_write2_b32 v119, v175, v147 offset0:6 offset1:7
	ds_write2_b32 v119, v203, v163 offset0:8 offset1:9
	ds_write2_b32 v119, v195, v166 offset0:10 offset1:11
	ds_write2_b32 v119, v185, v170 offset0:12 offset1:13
	ds_write2_b32 v119, v209, v161 offset0:14 offset1:15
